# P2 stage D2 (wave 5 column block): six serialised tile reads issued together with counted lgkmcnt; stacked
# speedup vs baseline: 1.0099x; 1.0068x over previous
.LBB0_451:
	s_andn2_b64 vcc, exec, s[92:93]
	s_cbranch_vccnz .LBB0_453
	v_and_b32_e32 v1, 48, v186
	v_add_u32_e32 v5, v4, v1
	v_lshlrev_b32_e32 v6, 6, v8
	v_add3_u32 v1, s25, v6, v1
	v_lshlrev_b32_e32 v9, 2, v2
	s_add_i32 s10, 0, 0x18000
	v_or_b32_e32 v252, 16, v8
	v_lshlrev_b32_e32 v253, 6, v252
	v_lshlrev_b32_e32 v10, 4, v2
	v_add3_u32 v253, s22, v253, v10
	ds_read_b128 v[228:231], v5 offset:8256
	ds_read_b128 v[232:235], v1 offset:2048
	ds_read_b128 v[236:239], v5 offset:12352
	ds_read_b128 v[240:243], v5 offset:12416
	ds_read_b128 v[244:247], v1 offset:3072
	ds_read_b128 v[248:251], v253
	v_lshrrev_b32_e32 v1, 3, v252
	v_lshlrev_b32_e32 v5, 1, v186
	v_and_b32_e32 v5, 14, v5
	s_waitcnt lgkmcnt(5)
	v_cvt_pk_bf16_f32 v6, v228, v229
	v_cvt_pk_bf16_f32 v7, v230, v231
	s_waitcnt lgkmcnt(4)
	v_cvt_pk_bf16_f32 v14, v232, v233
	v_cvt_pk_bf16_f32 v15, v234, v235
	s_waitcnt lgkmcnt(3)
	v_cvt_pk_bf16_f32 v16, v236, v237
	v_cvt_pk_bf16_f32 v17, v238, v239
	s_waitcnt lgkmcnt(2)
	v_cvt_pk_bf16_f32 v150, v240, v241
	v_cvt_pk_bf16_f32 v151, v242, v243
	s_waitcnt lgkmcnt(1)
	v_cvt_pk_bf16_f32 v152, v244, v245
	v_cvt_pk_bf16_f32 v153, v246, v247
	s_waitcnt lgkmcnt(0)
	v_cvt_pk_bf16_f32 v154, v248, v249
	v_cvt_pk_bf16_f32 v155, v250, v251
	s_nop 1
	v_mfma_f32_16x16x16_bf16 v[10:13], v[6:7], v[154:155], 0
	s_nop 7
	v_cvt_pk_bf16_f32 v6, v10, v11
	v_cvt_pk_bf16_f32 v7, v12, v13
	s_nop 1
	v_mfma_f32_16x16x16_bf16 v[10:13], v[14:15], v[6:7], 0
	s_nop 7
	v_xor_b32_e32 v14, 0x80000000, v12
	v_xor_b32_e32 v15, 0x80000000, v10
	v_and_or_b32 v12, v9, 4, v1
	v_xor_b32_e32 v6, 0x80000000, v11
	v_bfe_u32 v10, v15, 16, 1
	v_lshlrev_b32_e32 v11, 9, v2
	v_lshl_add_u32 v12, v12, 4, s10
	v_add3_u32 v10, v15, v10, s19
	v_add3_u32 v156, v12, v11, v5
	ds_write_b16_d16_hi v156, v10 offset:4096
	v_or_b32_e32 v10, 33, v9
	v_lshlrev_b32_e32 v12, 7, v10
	v_bitop3_b32 v10, v10, v1, 5 bitop3:0x6c
	v_bfe_u32 v11, v6, 16, 1
	v_lshl_add_u32 v10, v10, 4, s10
	v_add3_u32 v11, v6, v11, s19
	v_add3_u32 v10, v10, v12, v5
	ds_write_b16_d16_hi v10, v11
	v_or_b32_e32 v10, 34, v9
	v_lshlrev_b32_e32 v12, 7, v10
	v_bitop3_b32 v10, v10, v1, 6 bitop3:0x6c
	v_bfe_u32 v11, v14, 16, 1
	v_lshl_add_u32 v10, v10, 4, s10
	v_add3_u32 v11, v14, v11, s19
	v_add3_u32 v10, v10, v12, v5
	ds_write_b16_d16_hi v10, v11
	v_or_b32_e32 v10, 35, v9
	v_xor_b32_e32 v7, 0x80000000, v13
	v_lshlrev_b32_e32 v12, 7, v10
	v_bitop3_b32 v10, v10, v1, 7 bitop3:0x6c
	v_bfe_u32 v11, v7, 16, 1
	v_lshl_add_u32 v10, v10, 4, s10
	v_add3_u32 v11, v7, v11, s19
	v_add3_u32 v10, v10, v12, v5
	ds_write_b16_d16_hi v10, v11
	v_mfma_f32_16x16x16_bf16 v[10:13], v[16:17], v[154:155], 0
	v_cvt_pk_bf16_f32 v6, v15, v6
	v_cvt_pk_bf16_f32 v7, v14, v7
	s_nop 1
	v_mfma_f32_16x16x16_bf16 v[10:13], v[150:151], v[6:7], v[10:13]
	s_nop 7
	v_cvt_pk_bf16_f32 v6, v10, v11
	v_cvt_pk_bf16_f32 v7, v12, v13
	s_nop 1
	v_mfma_f32_16x16x16_bf16 v[10:13], v[152:153], v[6:7], 0
	s_nop 7
	v_xor_b32_e32 v10, 0x80000000, v10
	v_xor_b32_e32 v7, 0x80000000, v12
	v_bfe_u32 v12, v10, 16, 1
	v_xor_b32_e32 v11, 0x80000000, v11
	v_add3_u32 v10, v10, v12, s19
	ds_write_b16_d16_hi v156, v10 offset:6144
	v_or_b32_e32 v10, 49, v9
	v_bfe_u32 v12, v11, 16, 1
	v_add3_u32 v11, v11, v12, s19
	v_lshlrev_b32_e32 v12, 7, v10
	v_bitop3_b32 v10, v10, v1, 5 bitop3:0x6c
	v_lshl_add_u32 v10, v10, 4, s10
	v_add3_u32 v10, v10, v12, v5
	ds_write_b16_d16_hi v10, v11
	v_or_b32_e32 v10, 50, v9
	v_bfe_u32 v11, v7, 16, 1
	v_add3_u32 v7, v7, v11, s19
	v_lshlrev_b32_e32 v11, 7, v10
	v_bitop3_b32 v10, v10, v1, 6 bitop3:0x6c
	v_lshl_add_u32 v10, v10, 4, s10
	v_add3_u32 v10, v10, v11, v5
	v_xor_b32_e32 v6, 0x80000000, v13
	ds_write_b16_d16_hi v10, v7
	v_or_b32_e32 v7, 51, v9
	v_bfe_u32 v9, v6, 16, 1
	v_bitop3_b32 v1, v7, v1, 7 bitop3:0x6c
	v_add3_u32 v6, v6, v9, s19
	v_lshlrev_b32_e32 v9, 7, v7
	v_lshl_add_u32 v1, v1, 4, s10
	v_add3_u32 v1, v1, v9, v5
	ds_write_b16_d16_hi v1, v6
